# GDN chain compute step: att fragments beyond the causal limit (stored as zeros by prep) read and multiplied unconditionally - 7 wave-uniform branches and their mask rebuilds removed from the serial st
# baseline (speedup 1.0000x reference)
; __device__ void phase_gdn_chain(const Params& p, int l, char* smem, int vb, int nvb, int oz) {
;     ...
;                 bf16x8 sf[2];
; #pragma unroll
;                 for (int s = 0; s < 2; ++s) sf[s] = pack8(S[2 * s], S[2 * s + 1]);
;                 __builtin_amdgcn_sched_barrier(0);
;                 f32x4 vn[4];
; #pragma unroll
;                 for (int mt = 0; mt < 4; ++mt) {
;                     vn[mt] = (f32x4){lo16(uvw[mt][0]), hi16(uvw[mt][0]), lo16(uvw[mt][1]), hi16(uvw[mt][1])};
; #pragma unroll
;                     for (int s = 0; s < 2; ++s) vn[mt] = MFMA32(wa[mt][s], sf[s], vn[mt]);
;                 }
; #pragma unroll
;                 for (int mt = 0; mt < 4; ++mt)
; #pragma unroll
;                     for (int s = 0; s < 2; ++s)
;                         ka[mt][s] = *(const bf16x8*)(KT + (16 * mt + li) * LS + 32 * s + 8 * g);
;                 bf16x8 qa[4][2], aa[4][2];
;                 float eGc[4];
;                 if (need_o) {
; #pragma unroll
;                     for (int mt = 0; mt < 4; ++mt) {
;                         eGc[mt] = eG[16 * mt + li];
; #pragma unroll
;                         for (int s = 0; s < 2; ++s) {
;                             qa[mt][s] = *(const bf16x8*)(QQ + (16 * mt + li) * LS + 32 * s + 8 * g);
;                             if (!(dir ? (s == 0 && mt >= 2) : (s == 1 && mt < 2)))
;                                 aa[mt][s] = *(const bf16x8*)(AT + (16 * mt + li) * LS + 32 * s + 8 * g);
;                         }
;                     }
;                 }
;                 __builtin_amdgcn_sched_barrier(0);
;                 bf16x8 vf[2], vsf[2];
; #pragma unroll
;                 for (int s = 0; s < 2; ++s) {
;                     vf[s] = pack8(vn[2 * s], vn[2 * s + 1]);
;                     vsf[s] = pack8(vn[2 * s] * e0[s], vn[2 * s + 1] * e1[s]);
;                 }
; #pragma unroll
;                 for (int mt = 0; mt < 4; ++mt) {
;                     f32x4 acc = S[mt] * gt;
; #pragma unroll
;                     for (int s = 0; s < 2; ++s) acc = MFMA32(ka[mt][s], vsf[s], acc);
;                     S[mt] = acc;
;                 }
;                 ohave = need_o;
;                 if (need_o) {
;                     orow = c.rowbase + c.t0;
; #pragma unroll
;                     for (int mt = 0; mt < 4; ++mt) {
;                         f32x4 acc = {0.f, 0.f, 0.f, 0.f};
; #pragma unroll
.LBB0_398:
	s_or_b64 s[52:53], s[20:21], s[56:57]
	v_cvt_pk_bf16_f32 v84, v80, v81
	v_cvt_pk_bf16_f32 v85, v82, v83
	v_cvt_pk_bf16_f32 v86, v76, v77
	v_cvt_pk_bf16_f32 v87, v78, v79
	v_cvt_pk_bf16_f32 v88, v72, v73
	v_cvt_pk_bf16_f32 v89, v74, v75
	v_cvt_pk_bf16_f32 v90, v68, v69
	v_cvt_pk_bf16_f32 v91, v70, v71
	s_waitcnt lgkmcnt(0)
	v_lshlrev_b32_e32 v92, 16, v94
	v_and_b32_e32 v93, 0xffff0000, v94
	v_lshlrev_b32_e32 v94, 16, v95
	v_and_b32_e32 v95, 0xffff0000, v95
	ds_read_b128 v[152:155], v172 offset:18432
	ds_read_b128 v[148:151], v172 offset:18496
	v_mfma_f32_16x16x32_bf16 v[92:95], v[104:107], v[84:87], v[92:95]
	v_lshlrev_b32_e32 v104, 16, v96
	v_and_b32_e32 v105, 0xffff0000, v96
	v_lshlrev_b32_e32 v106, 16, v97
	v_and_b32_e32 v107, 0xffff0000, v97
	v_mfma_f32_16x16x32_bf16 v[92:95], v[112:115], v[88:91], v[92:95]
	v_lshlrev_b32_e32 v112, 16, v130
	v_and_b32_e32 v113, 0xffff0000, v130
	v_lshlrev_b32_e32 v114, 16, v131
	v_mfma_f32_16x16x32_bf16 v[96:99], v[124:127], v[84:87], v[104:107]
	v_and_b32_e32 v115, 0xffff0000, v131
	s_andn2_b64 vcc, exec, s[52:53]
	s_nop 0
	v_lshlrev_b32_e32 v104, 16, v128
	v_and_b32_e32 v105, 0xffff0000, v128
	v_lshlrev_b32_e32 v106, 16, v129
	v_and_b32_e32 v107, 0xffff0000, v129
	v_mfma_f32_16x16x32_bf16 v[112:115], v[144:147], v[84:87], v[112:115]
	s_nop 0
	v_mfma_f32_16x16x32_bf16 v[104:107], v[136:139], v[84:87], v[104:107]
	v_mfma_f32_16x16x32_bf16 v[96:99], v[132:135], v[88:91], v[96:99]
	v_mfma_f32_16x16x32_bf16 v[104:107], v[140:143], v[88:91], v[104:107]
	ds_read_b128 v[140:143], v172 offset:20736
	ds_read_b128 v[144:147], v172 offset:20800
	ds_read_b128 v[132:135], v172 offset:23040
	ds_read_b128 v[136:139], v172 offset:23104
	ds_read_b128 v[128:131], v172 offset:25344
	ds_read_b128 v[124:127], v172 offset:25408
	v_cndmask_b32_e64 v172, 0, 1, s[52:53]
	v_mfma_f32_16x16x32_bf16 v[112:115], v[174:177], v[88:91], v[112:115]
	v_cmp_ne_u32_e64 s[42:43], 1, v172
	s_cbranch_vccnz .LBB0_408
	v_lshl_add_u32 v52, v188, 2, s0
	v_lshl_add_u32 v64, v209, 1, v173
	ds_read_b32 v206, v52 offset:45056
	ds_read_b128 v[28:31], v64 offset:9216
	ds_read_b128 v[20:23], v64 offset:27648
	ds_read_b128 v[16:19], v64 offset:27712
	ds_read_b128 v[24:27], v64 offset:9280
	ds_read_b32 v208, v52 offset:45120
	ds_read_b128 v[40:43], v64 offset:11520
	ds_read_b128 v[36:39], v64 offset:29952
	ds_read_b128 v[32:35], v64 offset:30016
	ds_read_b128 v[12:15], v64 offset:11584
	ds_read_b32 v210, v52 offset:45184
	ds_read_b128 v[44:47], v64 offset:32256
	ds_read_b128 v[8:11], v64 offset:13824
	ds_read_b128 v[48:51], v64 offset:32320
	ds_read_b128 v[56:59], v64 offset:13888
	ds_read_b32 v212, v52 offset:45248
	ds_read_b128 v[52:55], v64 offset:34560
	ds_read_b128 v[4:7], v64 offset:16128
	ds_read_b128 v[60:63], v64 offset:34624
	ds_read_b128 v[64:67], v64 offset:16192
.LBB0_408:
	v_pk_mul_f32 v[122:123], v[122:123], v[94:95]
	v_pk_mul_f32 v[120:121], v[120:121], v[92:93]
	v_pk_mul_f32 v[174:175], v[118:119], v[98:99]
	v_pk_mul_f32 v[118:119], v[116:117], v[96:97]
	v_cvt_pk_bf16_f32 v116, v120, v121
	v_cvt_pk_bf16_f32 v117, v122, v123
	v_cvt_pk_bf16_f32 v118, v118, v119
	v_cvt_pk_bf16_f32 v119, v174, v175
	v_pk_mul_f32 v[82:83], v[82:83], v[2:3] op_sel_hi:[1,0]
	v_pk_mul_f32 v[80:81], v[80:81], v[2:3] op_sel_hi:[1,0]
	v_pk_mul_f32 v[78:79], v[78:79], v[2:3] op_sel_hi:[1,0]
	v_pk_mul_f32 v[76:77], v[76:77], v[2:3] op_sel_hi:[1,0]
	v_pk_mul_f32 v[74:75], v[74:75], v[2:3] op_sel_hi:[1,0]
	v_pk_mul_f32 v[72:73], v[72:73], v[2:3] op_sel_hi:[1,0]
	v_pk_mul_f32 v[70:71], v[70:71], v[2:3] op_sel_hi:[1,0]
	v_pk_mul_f32 v[68:69], v[68:69], v[2:3] op_sel_hi:[1,0]
	s_waitcnt lgkmcnt(7)
	v_mfma_f32_16x16x32_bf16 v[80:83], v[152:155], v[116:119], v[80:83]
	v_mul_f32_e64 v110, v110, v106
	v_mul_f32_e64 v111, v111, v107
	v_pk_mul_f32 v[108:109], v[108:109], v[104:105]
	v_pk_mul_f32 v[120:121], v[102:103], v[114:115]
	s_waitcnt lgkmcnt(5)
	v_mfma_f32_16x16x32_bf16 v[76:79], v[140:143], v[116:119], v[76:79]
	v_mul_f32_e64 v102, v100, v112
	v_mul_f32_e64 v103, v101, v113
	v_cvt_pk_bf16_f32 v100, v108, v109
	v_cvt_pk_bf16_f32 v101, v110, v111
	s_waitcnt lgkmcnt(3)
	v_mfma_f32_16x16x32_bf16 v[72:75], v[132:135], v[116:119], v[72:75]
	v_cvt_pk_bf16_f32 v102, v102, v103
	v_cvt_pk_bf16_f32 v103, v120, v121
	s_and_b64 vcc, exec, s[42:43]
	s_waitcnt lgkmcnt(1)
	v_mfma_f32_16x16x32_bf16 v[68:71], v[128:131], v[116:119], v[68:71]
	v_mfma_f32_16x16x32_bf16 v[80:83], v[148:151], v[100:103], v[80:83]
	v_mfma_f32_16x16x32_bf16 v[76:79], v[144:147], v[100:103], v[76:79]
	v_mfma_f32_16x16x32_bf16 v[72:75], v[136:139], v[100:103], v[72:75]
	s_waitcnt lgkmcnt(0)
	v_mfma_f32_16x16x32_bf16 v[68:71], v[124:127], v[100:103], v[68:71]
	s_cbranch_vccnz .LBB0_395
	v_cvt_pk_bf16_f32 v100, v104, v105
	v_cvt_pk_bf16_f32 v101, v106, v107
	v_cvt_pk_bf16_f32 v102, v112, v113
	v_cvt_pk_bf16_f32 v103, v114, v115
	v_cvt_pk_bf16_f32 v92, v92, v93
	v_cvt_pk_bf16_f32 v93, v94, v95
	v_cvt_pk_bf16_f32 v94, v96, v97
	v_cvt_pk_bf16_f32 v95, v98, v99
	v_mfma_f32_16x16x32_bf16 v[96:99], v[84:87], v[20:23], 0
	v_mfma_f32_16x16x32_bf16 v[104:107], v[84:87], v[36:39], 0
	v_mfma_f32_16x16x32_bf16 v[108:111], v[84:87], v[44:47], 0
	v_mfma_f32_16x16x32_bf16 v[112:115], v[84:87], v[52:55], 0
	v_mfma_f32_16x16x32_bf16 v[96:99], v[88:91], v[16:19], v[96:99]
	v_mfma_f32_16x16x32_bf16 v[104:107], v[88:91], v[32:35], v[104:107]
	v_mfma_f32_16x16x32_bf16 v[108:111], v[88:91], v[48:51], v[108:111]
	v_mfma_f32_16x16x32_bf16 v[112:115], v[88:91], v[60:63], v[112:115]
	s_nop 4
	v_pk_mul_f32 v[98:99], v[206:207], v[98:99] op_sel_hi:[0,1]
	v_pk_mul_f32 v[96:97], v[206:207], v[96:97] op_sel_hi:[0,1]
	v_pk_mul_f32 v[106:107], v[208:209], v[106:107] op_sel_hi:[0,1]
	v_pk_mul_f32 v[104:105], v[208:209], v[104:105] op_sel_hi:[0,1]
	v_pk_mul_f32 v[110:111], v[210:211], v[110:111] op_sel_hi:[0,1]
	v_pk_mul_f32 v[108:109], v[210:211], v[108:109] op_sel_hi:[0,1]
	v_mul_f32_e64 v114, v212, v114
	v_mul_f32_e64 v115, v212, v115
	v_pk_mul_f32 v[112:113], v[212:213], v[112:113] op_sel_hi:[0,1]
	v_mfma_f32_16x16x32_bf16 v[96:99], v[92:95], v[28:31], v[96:99]
	v_mfma_f32_16x16x32_bf16 v[104:107], v[92:95], v[40:43], v[104:107]
	v_mfma_f32_16x16x32_bf16 v[108:111], v[92:95], v[8:11], v[108:111]
	v_mfma_f32_16x16x32_bf16 v[112:115], v[92:95], v[4:7], v[112:115]
	v_mfma_f32_16x16x32_bf16 v[108:111], v[100:103], v[56:59], v[108:111]
	v_mfma_f32_16x16x32_bf16 v[112:115], v[100:103], v[64:67], v[112:115]
	v_mfma_f32_16x16x32_bf16 v[96:99], v[100:103], v[24:27], v[96:99]
	v_mfma_f32_16x16x32_bf16 v[104:107], v[100:103], v[12:15], v[104:107]
	s_branch .LBB0_394
